# loop-header address bookkeeping hoisted into the previous MFMA run and spread over the MFMA gaps
# speedup vs baseline: 1.0305x; 1.0051x over previous
.LBB2_33:
	s_waitcnt vmcnt(6)
	s_barrier
	s_setprio 1
	v_mfma_i32_16x16x64_i8 v[48:51], v[144:147], v[184:187], v[48:51]
	s_add_i32 s74, s74, 2
	v_mfma_i32_16x16x64_i8 v[40:43], v[148:151], v[184:187], v[40:43]
	s_add_u32 s70, s70, 0x100
	s_addc_u32 s71, s71, 0
	v_mfma_i32_16x16x64_i8 v[32:35], v[144:147], v[172:175], v[32:35]
	s_add_u32 s72, s72, 0x100
	s_addc_u32 s73, s73, 0
	v_mfma_i32_16x16x64_i8 v[24:27], v[148:151], v[172:175], v[24:27]
	s_cmp_gt_u32 s74, 13
	v_mfma_i32_16x16x64_i8 v[16:19], v[144:147], v[168:171], v[16:19]
	v_mfma_i32_16x16x64_i8 v[8:11], v[148:151], v[168:171], v[8:11]
	v_mfma_i32_16x16x64_i8 v[4:7], v[144:147], v[160:163], v[4:7]
	v_mfma_i32_16x16x64_i8 v[0:3], v[148:151], v[160:163], v[0:3]
	v_mfma_i32_16x16x64_i8 v[48:51], v[156:159], v[188:191], v[48:51]
	v_mfma_i32_16x16x64_i8 v[40:43], v[152:155], v[188:191], v[40:43]
	v_mfma_i32_16x16x64_i8 v[32:35], v[156:159], v[176:179], v[32:35]
	v_mfma_i32_16x16x64_i8 v[24:27], v[152:155], v[176:179], v[24:27]
	v_mfma_i32_16x16x64_i8 v[16:19], v[156:159], v[180:183], v[16:19]
	v_mfma_i32_16x16x64_i8 v[8:11], v[152:155], v[180:183], v[8:11]
	v_mfma_i32_16x16x64_i8 v[4:7], v[156:159], v[164:167], v[4:7]
	v_mfma_i32_16x16x64_i8 v[0:3], v[152:155], v[164:167], v[0:3]
	s_setprio 0
	s_barrier
	s_cbranch_scc1 .LBB2_50

.LBB2_42:
	s_barrier
	s_setprio 1
	v_mfma_i32_16x16x64_i8 v[48:51], v[128:131], v[184:187], v[48:51]
	s_add_i32 s5, 0, 0x18000
	v_add_u32_e32 v210, s5, v199
	v_mfma_i32_16x16x64_i8 v[40:43], v[132:135], v[184:187], v[40:43]
	v_add_u32_e32 v211, s5, v200
	v_mfma_i32_16x16x64_i8 v[32:35], v[128:131], v[172:175], v[32:35]
	v_mfma_i32_16x16x64_i8 v[24:27], v[132:135], v[172:175], v[24:27]
	v_mfma_i32_16x16x64_i8 v[16:19], v[128:131], v[168:171], v[16:19]
	v_mfma_i32_16x16x64_i8 v[8:11], v[132:135], v[168:171], v[8:11]
	v_mfma_i32_16x16x64_i8 v[4:7], v[128:131], v[160:163], v[4:7]
	v_mfma_i32_16x16x64_i8 v[0:3], v[132:135], v[160:163], v[0:3]
	v_mfma_i32_16x16x64_i8 v[48:51], v[140:143], v[188:191], v[48:51]
	v_mfma_i32_16x16x64_i8 v[40:43], v[136:139], v[188:191], v[40:43]
	v_mfma_i32_16x16x64_i8 v[32:35], v[140:143], v[176:179], v[32:35]
	v_mfma_i32_16x16x64_i8 v[24:27], v[136:139], v[176:179], v[24:27]
	v_mfma_i32_16x16x64_i8 v[16:19], v[140:143], v[180:183], v[16:19]
	v_mfma_i32_16x16x64_i8 v[8:11], v[136:139], v[180:183], v[8:11]
	v_mfma_i32_16x16x64_i8 v[4:7], v[140:143], v[164:167], v[4:7]
	v_mfma_i32_16x16x64_i8 v[0:3], v[136:139], v[164:167], v[0:3]
	s_setprio 0
	s_barrier
	ds_read_b128 v[128:131], v210
	ds_read_b128 v[132:135], v210 offset:2048
	ds_read_b128 v[140:143], v211
	ds_read_b128 v[136:139], v211 offset:2048
	ds_read_b128 v[184:187], v205 offset:32768
	ds_read_b128 v[172:175], v205 offset:34816
	ds_read_b128 v[188:191], v206 offset:32768
	ds_read_b128 v[176:179], v206 offset:34816
	ds_read_b128 v[168:171], v205 offset:36864
	ds_read_b128 v[160:163], v205 offset:38912
	ds_read_b128 v[180:183], v206 offset:36864
	ds_read_b128 v[164:167], v206 offset:38912
	s_and_b64 vcc, exec, s[0:1]
	s_cbranch_vccnz .LBB2_44
	s_add_u32 s76, s4, 0x40000
	s_addc_u32 s5, s17, 0
	s_and_b32 s77, s5, 0xffff
	s_mov_b32 s78, s6
	s_mov_b32 s79, s7
	s_mov_b32 m0, s44
	s_nop 0
	buffer_load_dwordx4 v193, s[76:79], 0 offen lds
	s_mov_b32 m0, s45
	s_nop 0
	buffer_load_dwordx4 v197, s[76:79], 0 offen lds

.Lp2_sum_skip:
	s_barrier
	buffer_load_dwordx4 v194, s[12:15], 0 offen lds
	s_mov_b32 m0, s41
	v_lshrrev_b32_e32 v2, 4, v0
	buffer_load_dwordx4 v196, s[12:15], 0 offen lds
	s_add_u32 s12, s16, 0x80
	s_addc_u32 s0, s9, 0
	s_add_i32 s42, s31, 0x8000
	s_and_b32 s13, s0, 0xffff
	s_mov_b32 m0, s42
	s_add_i32 s43, s31, 0xa000
	buffer_load_dwordx4 v1, s[12:15], 0 offen lds
	s_mov_b32 m0, s43
	v_and_b32_e32 v197, 15, v0
	buffer_load_dwordx4 v195, s[12:15], 0 offen lds
	s_add_u32 s12, s8, 0x10080
	s_addc_u32 s0, s25, 0
	s_add_i32 s44, s31, 0x1c000
	s_and_b32 s13, s0, 0xffff
	s_mov_b32 m0, s44
	s_add_i32 s45, s31, 0x1e000
	buffer_load_dwordx4 v194, s[12:15], 0 offen lds
	s_mov_b32 m0, s45
	s_and_b32 s0, s2, 1
	buffer_load_dwordx4 v196, s[12:15], 0 offen lds
	s_lshl_b32 s0, s0, 23
	s_lshl_b32 s1, s26, 21
	v_bfe_u32 v3, v0, 1, 3
	s_or_b32 s0, s0, s1
	v_bitop3_b32 v2, v2, v3, 3 bitop3:0x6c
	v_lshlrev_b32_e32 v3, 7, v197
	s_add_i32 s46, s31, 0xc000
	s_add_i32 s47, s31, 0xe000
	s_or_b32 s0, s27, s0
	v_lshlrev_b32_e32 v2, 4, v2
	v_lshl_or_b32 v4, s28, 13, v3
	v_lshl_or_b32 v3, s39, 12, v3
	s_waitcnt vmcnt(6)
	s_add_u32 s48, s20, s0
	v_or_b32_e32 v5, v4, v2
	v_bitop3_b32 v4, v4, 64, v2 bitop3:0x36
	v_or_b32_e32 v198, v3, v2
	v_bitop3_b32 v199, v3, 64, v2 bitop3:0x36
	s_addc_u32 s49, s21, 0
	v_mov_b32_e32 v66, 0
	s_add_i32 s0, 0, 0x10000
	s_add_i32 s1, 0, 0x14000
	s_mov_b32 s50, -2
	s_mov_b64 s[10:11], 0
	v_add_u32_e32 v200, 0, v5
	v_add_u32_e32 v201, 0, v4
	v_mov_b32_e32 v67, v66
	v_mov_b32_e32 v68, v66
	v_mov_b32_e32 v69, v66
	v_mov_b32_e32 v70, v66
	v_mov_b32_e32 v71, v66
	v_mov_b32_e32 v72, v66
	v_mov_b32_e32 v73, v66
	v_mov_b32_e32 v82, v66
	v_mov_b32_e32 v83, v66
	v_mov_b32_e32 v84, v66
	v_mov_b32_e32 v85, v66
	v_mov_b32_e32 v86, v66
	v_mov_b32_e32 v87, v66
	v_mov_b32_e32 v88, v66
	v_mov_b32_e32 v89, v66
	v_mov_b32_e32 v98, v66
	v_mov_b32_e32 v99, v66
	v_mov_b32_e32 v100, v66
	v_mov_b32_e32 v101, v66
	v_mov_b32_e32 v102, v66
	v_mov_b32_e32 v103, v66
	v_mov_b32_e32 v104, v66
	v_mov_b32_e32 v105, v66
	v_mov_b32_e32 v114, v66
	v_mov_b32_e32 v115, v66
	v_mov_b32_e32 v116, v66
	v_mov_b32_e32 v117, v66
	v_mov_b32_e32 v118, v66
	v_mov_b32_e32 v119, v66
	v_mov_b32_e32 v120, v66
	v_mov_b32_e32 v121, v66
	v_mov_b32_e32 v74, v66
	v_mov_b32_e32 v75, v66
	v_mov_b32_e32 v76, v66
	v_mov_b32_e32 v77, v66
	v_mov_b32_e32 v78, v66
	v_mov_b32_e32 v79, v66
	v_mov_b32_e32 v80, v66
	v_mov_b32_e32 v81, v66
	v_mov_b32_e32 v90, v66
	v_mov_b32_e32 v91, v66
	v_mov_b32_e32 v92, v66
	v_mov_b32_e32 v93, v66
	v_mov_b32_e32 v94, v66
	v_mov_b32_e32 v95, v66
	v_mov_b32_e32 v96, v66
	v_mov_b32_e32 v97, v66
	v_mov_b32_e32 v106, v66
	v_mov_b32_e32 v107, v66
	v_mov_b32_e32 v108, v66
	v_mov_b32_e32 v109, v66
	v_mov_b32_e32 v110, v66
	v_mov_b32_e32 v111, v66
	v_mov_b32_e32 v112, v66
	v_mov_b32_e32 v113, v66
	v_mov_b32_e32 v122, v66
	v_mov_b32_e32 v123, v66
	v_mov_b32_e32 v124, v66
	v_mov_b32_e32 v125, v66
	v_mov_b32_e32 v126, v66
	v_mov_b32_e32 v127, v66
	v_mov_b32_e32 v128, v66
	v_mov_b32_e32 v129, v66
	v_mov_b32_e32 v130, v66
	v_mov_b32_e32 v131, v66
	v_mov_b32_e32 v132, v66
	v_mov_b32_e32 v133, v66
	v_mov_b32_e32 v134, v66
	v_mov_b32_e32 v135, v66
	v_mov_b32_e32 v136, v66
	v_mov_b32_e32 v137, v66
	v_mov_b32_e32 v146, v66
	v_mov_b32_e32 v147, v66
	v_mov_b32_e32 v148, v66
	v_mov_b32_e32 v149, v66
	v_mov_b32_e32 v150, v66
	v_mov_b32_e32 v151, v66
	v_mov_b32_e32 v152, v66
	v_mov_b32_e32 v153, v66
	v_mov_b32_e32 v162, v66
	v_mov_b32_e32 v163, v66
	v_mov_b32_e32 v164, v66
	v_mov_b32_e32 v165, v66
	v_mov_b32_e32 v166, v66
	v_mov_b32_e32 v167, v66
	v_mov_b32_e32 v168, v66
	v_mov_b32_e32 v169, v66
	v_mov_b32_e32 v178, v66
	v_mov_b32_e32 v179, v66
	v_mov_b32_e32 v180, v66
	v_mov_b32_e32 v181, v66
	v_mov_b32_e32 v182, v66
	v_mov_b32_e32 v183, v66
	v_mov_b32_e32 v184, v66
	v_mov_b32_e32 v185, v66
	v_mov_b32_e32 v138, v66
	v_mov_b32_e32 v139, v66
	v_mov_b32_e32 v140, v66
	v_mov_b32_e32 v141, v66
	v_mov_b32_e32 v142, v66
	v_mov_b32_e32 v143, v66
	v_mov_b32_e32 v144, v66
	v_mov_b32_e32 v145, v66
	v_mov_b32_e32 v154, v66
	v_mov_b32_e32 v155, v66
	v_mov_b32_e32 v156, v66
	v_mov_b32_e32 v157, v66
	v_mov_b32_e32 v158, v66
	v_mov_b32_e32 v159, v66
	v_mov_b32_e32 v160, v66
	v_mov_b32_e32 v161, v66
	v_mov_b32_e32 v170, v66
	v_mov_b32_e32 v171, v66
	v_mov_b32_e32 v172, v66
	v_mov_b32_e32 v173, v66
	v_mov_b32_e32 v174, v66
	v_mov_b32_e32 v175, v66
	v_mov_b32_e32 v176, v66
	v_mov_b32_e32 v177, v66
	v_mov_b32_e32 v186, v66
	v_mov_b32_e32 v187, v66
	v_mov_b32_e32 v188, v66
	v_mov_b32_e32 v189, v66
	v_mov_b32_e32 v190, v66
	v_mov_b32_e32 v191, v66
	v_mov_b32_e32 v192, v66
	v_mov_b32_e32 v193, v66
	v_bfe_u32 v202, v0, 4, 2
	v_add_u32_e32 v203, s0, v198
	v_add_u32_e32 v204, s0, v199
	v_add_u32_e32 v205, s1, v198
	v_add_u32_e32 v206, s1, v199
	s_barrier
	s_cmpk_eq_i32 s10, 0x700
	s_cselect_b64 s[18:19], -1, 0
	s_cmpk_lg_i32 s10, 0x700
	s_cselect_b64 s[26:27], -1, 0
	s_add_u32 s54, s48, s10
	s_addc_u32 s55, s49, s11
	s_add_u32 s51, s8, s10
	s_addc_u32 s52, s25, s11
	s_add_u32 s20, s51, 0x100
	s_addc_u32 s53, s52, 0
	s_add_u32 s12, s54, 0x100080
	s_addc_u32 s0, s55, 0
	s_and_b32 s13, s0, 0xffff
	s_branch .LBB3_4
.LBB3_3:
	s_waitcnt vmcnt(6)
	s_barrier
	s_setprio 1
	v_mfma_f32_16x16x128_f8f6f4 v[118:121], v[26:33], v[58:65], v[118:121]
	s_add_i32 s50, s50, 2
	s_add_u32 s10, s10, 0x100
	s_addc_u32 s11, s11, 0
	v_mfma_f32_16x16x128_f8f6f4 v[114:117], v[18:25], v[58:65], v[114:117]
	s_cmpk_eq_i32 s10, 0x700
	s_cselect_b64 s[18:19], -1, 0
	s_cmpk_lg_i32 s10, 0x700
	s_cselect_b64 s[26:27], -1, 0
	v_mfma_f32_16x16x128_f8f6f4 v[102:105], v[26:33], v[50:57], v[102:105]
	s_add_u32 s54, s48, s10
	s_addc_u32 s55, s49, s11
	s_add_u32 s51, s8, s10
	s_addc_u32 s52, s25, s11
	v_mfma_f32_16x16x128_f8f6f4 v[98:101], v[18:25], v[50:57], v[98:101]
	s_add_u32 s20, s51, 0x100
	s_addc_u32 s53, s52, 0
	s_add_u32 s12, s54, 0x100080
	s_addc_u32 s0, s55, 0
	v_mfma_f32_16x16x128_f8f6f4 v[86:89], v[26:33], v[42:49], v[86:89]
	s_and_b32 s13, s0, 0xffff
	s_cmp_gt_u32 s50, 13
	v_mfma_f32_16x16x128_f8f6f4 v[82:85], v[18:25], v[42:49], v[82:85]
	v_mfma_f32_16x16x128_f8f6f4 v[70:73], v[26:33], v[34:41], v[70:73]
	v_mfma_f32_16x16x128_f8f6f4 v[66:69], v[18:25], v[34:41], v[66:69]
	s_setprio 0
	s_barrier
	s_cbranch_scc1 .LBB3_20
.LBB3_4:
	ds_read_b128 v[2:5], v203
	ds_read_b128 v[10:13], v203 offset:2048
	ds_read_b128 v[6:9], v204
	ds_read_b128 v[14:17], v204 offset:2048
	s_mov_b32 m0, s46
	ds_read_b128 v[58:61], v200
	ds_read_b128 v[50:53], v200 offset:2048
	ds_read_b128 v[62:65], v201
	ds_read_b128 v[54:57], v201 offset:2048
	ds_read_b128 v[42:45], v200 offset:4096
	ds_read_b128 v[34:37], v200 offset:6144
	ds_read_b128 v[46:49], v201 offset:4096
	ds_read_b128 v[38:41], v201 offset:6144
	buffer_load_dwordx4 v1, s[12:15], 0 offen lds
	s_mov_b32 m0, s47
	s_nop 0
	buffer_load_dwordx4 v195, s[12:15], 0 offen lds
	s_waitcnt lgkmcnt(8)
	s_barrier
	s_waitcnt lgkmcnt(0)
	s_setprio 1
	v_mfma_f32_16x16x128_f8f6f4 v[190:193], v[2:9], v[58:65], v[190:193]
	v_mfma_f32_16x16x128_f8f6f4 v[186:189], v[10:17], v[58:65], v[186:189]
	v_mfma_f32_16x16x128_f8f6f4 v[174:177], v[2:9], v[50:57], v[174:177]
	v_mfma_f32_16x16x128_f8f6f4 v[170:173], v[10:17], v[50:57], v[170:173]
	v_mfma_f32_16x16x128_f8f6f4 v[158:161], v[2:9], v[42:49], v[158:161]
	v_mfma_f32_16x16x128_f8f6f4 v[154:157], v[10:17], v[42:49], v[154:157]
	v_mfma_f32_16x16x128_f8f6f4 v[142:145], v[2:9], v[34:41], v[142:145]
	v_mfma_f32_16x16x128_f8f6f4 v[138:141], v[10:17], v[34:41], v[138:141]
	s_setprio 0
	s_barrier
	ds_read_b128 v[26:29], v205
	ds_read_b128 v[18:21], v205 offset:2048
	ds_read_b128 v[30:33], v206
	ds_read_b128 v[22:25], v206 offset:2048
	s_and_b64 vcc, exec, s[18:19]
	s_cbranch_vccnz .LBB3_6
	s_and_b32 s21, s53, 0xffff
	s_mov_b32 s22, s14
	s_mov_b32 s23, s15
	s_mov_b32 m0, s33
	s_nop 0
	buffer_load_dwordx4 v194, s[20:23], 0 offen lds
	s_mov_b32 m0, s34
	s_nop 0
	buffer_load_dwordx4 v196, s[20:23], 0 offen lds

.LBB4_12:
	s_and_b32 s33, s0, 3
	s_add_u32 s12, s8, 0x80
	s_addc_u32 s0, s3, 0
	s_add_i32 s36, s7, 0x18000
	s_and_b32 s13, s0, 0xffff
	s_mov_b32 m0, s36
	s_add_i32 s37, s7, 0x1a000
	s_waitcnt vmcnt(4)
	s_barrier
	buffer_load_dwordx4 v193, s[12:15], 0 offen lds
	s_mov_b32 m0, s37
	v_lshrrev_b32_e32 v1, 4, v0
	buffer_load_dwordx4 v195, s[12:15], 0 offen lds
	s_add_u32 s12, s16, 0x80
	s_addc_u32 s0, s9, 0
	s_add_i32 s38, s7, 0x8000
	s_and_b32 s13, s0, 0xffff
	s_mov_b32 m0, s38
	s_add_i32 s39, s7, 0xa000
	buffer_load_dwordx4 v192, s[12:15], 0 offen lds
	s_mov_b32 m0, s39
	v_and_b32_e32 v196, 15, v0
	buffer_load_dwordx4 v194, s[12:15], 0 offen lds
	s_add_u32 s12, s8, 0x4080
	s_addc_u32 s0, s3, 0
	s_add_i32 s40, s7, 0x1c000
	s_and_b32 s13, s0, 0xffff
	s_mov_b32 m0, s40
	s_add_i32 s41, s7, 0x1e000
	buffer_load_dwordx4 v193, s[12:15], 0 offen lds
	s_mov_b32 m0, s41
	v_bfe_u32 v197, v0, 4, 2
	buffer_load_dwordx4 v195, s[12:15], 0 offen lds
	v_bfe_u32 v0, v0, 1, 3
	v_bitop3_b32 v0, v1, v0, 3 bitop3:0x6c
	v_lshlrev_b32_e32 v1, 7, v196
	v_lshlrev_b32_e32 v0, 4, v0
	v_lshl_or_b32 v2, s27, 13, v1
	v_lshl_or_b32 v1, s33, 12, v1
	s_waitcnt vmcnt(6)
	v_or_b32_e32 v3, v2, v0
	v_or_b32_e32 v198, v1, v0
	v_bitop3_b32 v2, v2, 64, v0 bitop3:0x36
	v_bitop3_b32 v199, v1, 64, v0 bitop3:0x36
	v_mov_b32_e32 v64, 0
	s_add_i32 s0, 0, 0x10000
	s_add_i32 s1, 0, 0x14000
	s_add_i32 s42, s7, 0xc000
	s_add_i32 s43, s7, 0xe000
	s_mov_b32 s44, -2
	s_mov_b64 s[10:11], 0
	v_add_u32_e32 v200, 0, v3
	v_add_u32_e32 v201, 0, v2
	s_add_i32 s45, 0, 0x18000
	v_mov_b32_e32 v65, v64
	v_mov_b32_e32 v66, v64
	v_mov_b32_e32 v67, v64
	v_mov_b32_e32 v68, v64
	v_mov_b32_e32 v69, v64
	v_mov_b32_e32 v70, v64
	v_mov_b32_e32 v71, v64
	v_mov_b32_e32 v80, v64
	v_mov_b32_e32 v81, v64
	v_mov_b32_e32 v82, v64
	v_mov_b32_e32 v83, v64
	v_mov_b32_e32 v84, v64
	v_mov_b32_e32 v85, v64
	v_mov_b32_e32 v86, v64
	v_mov_b32_e32 v87, v64
	v_mov_b32_e32 v96, v64
	v_mov_b32_e32 v97, v64
	v_mov_b32_e32 v98, v64
	v_mov_b32_e32 v99, v64
	v_mov_b32_e32 v100, v64
	v_mov_b32_e32 v101, v64
	v_mov_b32_e32 v102, v64
	v_mov_b32_e32 v103, v64
	v_mov_b32_e32 v112, v64
	v_mov_b32_e32 v113, v64
	v_mov_b32_e32 v114, v64
	v_mov_b32_e32 v115, v64
	v_mov_b32_e32 v116, v64
	v_mov_b32_e32 v117, v64
	v_mov_b32_e32 v118, v64
	v_mov_b32_e32 v119, v64
	v_mov_b32_e32 v72, v64
	v_mov_b32_e32 v73, v64
	v_mov_b32_e32 v74, v64
	v_mov_b32_e32 v75, v64
	v_mov_b32_e32 v76, v64
	v_mov_b32_e32 v77, v64
	v_mov_b32_e32 v78, v64
	v_mov_b32_e32 v79, v64
	v_mov_b32_e32 v88, v64
	v_mov_b32_e32 v89, v64
	v_mov_b32_e32 v90, v64
	v_mov_b32_e32 v91, v64
	v_mov_b32_e32 v92, v64
	v_mov_b32_e32 v93, v64
	v_mov_b32_e32 v94, v64
	v_mov_b32_e32 v95, v64
	v_mov_b32_e32 v104, v64
	v_mov_b32_e32 v105, v64
	v_mov_b32_e32 v106, v64
	v_mov_b32_e32 v107, v64
	v_mov_b32_e32 v108, v64
	v_mov_b32_e32 v109, v64
	v_mov_b32_e32 v110, v64
	v_mov_b32_e32 v111, v64
	v_mov_b32_e32 v120, v64
	v_mov_b32_e32 v121, v64
	v_mov_b32_e32 v122, v64
	v_mov_b32_e32 v123, v64
	v_mov_b32_e32 v124, v64
	v_mov_b32_e32 v125, v64
	v_mov_b32_e32 v126, v64
	v_mov_b32_e32 v127, v64
	v_mov_b32_e32 v128, v64
	v_mov_b32_e32 v129, v64
	v_mov_b32_e32 v130, v64
	v_mov_b32_e32 v131, v64
	v_mov_b32_e32 v132, v64
	v_mov_b32_e32 v133, v64
	v_mov_b32_e32 v134, v64
	v_mov_b32_e32 v135, v64
	v_mov_b32_e32 v144, v64
	v_mov_b32_e32 v145, v64
	v_mov_b32_e32 v146, v64
	v_mov_b32_e32 v147, v64
	v_mov_b32_e32 v148, v64
	v_mov_b32_e32 v149, v64
	v_mov_b32_e32 v150, v64
	v_mov_b32_e32 v151, v64
	v_mov_b32_e32 v160, v64
	v_mov_b32_e32 v161, v64
	v_mov_b32_e32 v162, v64
	v_mov_b32_e32 v163, v64
	v_mov_b32_e32 v164, v64
	v_mov_b32_e32 v165, v64
	v_mov_b32_e32 v166, v64
	v_mov_b32_e32 v167, v64
	v_mov_b32_e32 v176, v64
	v_mov_b32_e32 v177, v64
	v_mov_b32_e32 v178, v64
	v_mov_b32_e32 v179, v64
	v_mov_b32_e32 v180, v64
	v_mov_b32_e32 v181, v64
	v_mov_b32_e32 v182, v64
	v_mov_b32_e32 v183, v64
	v_mov_b32_e32 v136, v64
	v_mov_b32_e32 v137, v64
	v_mov_b32_e32 v138, v64
	v_mov_b32_e32 v139, v64
	v_mov_b32_e32 v140, v64
	v_mov_b32_e32 v141, v64
	v_mov_b32_e32 v142, v64
	v_mov_b32_e32 v143, v64
	v_mov_b32_e32 v152, v64
	v_mov_b32_e32 v153, v64
	v_mov_b32_e32 v154, v64
	v_mov_b32_e32 v155, v64
	v_mov_b32_e32 v156, v64
	v_mov_b32_e32 v157, v64
	v_mov_b32_e32 v158, v64
	v_mov_b32_e32 v159, v64
	v_mov_b32_e32 v168, v64
	v_mov_b32_e32 v169, v64
	v_mov_b32_e32 v170, v64
	v_mov_b32_e32 v171, v64
	v_mov_b32_e32 v172, v64
	v_mov_b32_e32 v173, v64
	v_mov_b32_e32 v174, v64
	v_mov_b32_e32 v175, v64
	v_mov_b32_e32 v184, v64
	v_mov_b32_e32 v185, v64
	v_mov_b32_e32 v186, v64
	v_mov_b32_e32 v187, v64
	v_mov_b32_e32 v188, v64
	v_mov_b32_e32 v189, v64
	v_mov_b32_e32 v190, v64
	v_mov_b32_e32 v191, v64
	v_add_u32_e32 v202, s0, v198
	v_add_u32_e32 v203, s0, v199
	v_add_u32_e32 v204, s1, v198
	v_add_u32_e32 v205, s1, v199
	s_barrier
	s_cmpk_eq_i32 s10, 0x700
	s_cselect_b64 s[18:19], -1, 0
	s_cmpk_lg_i32 s10, 0x700
	s_cselect_b64 s[24:25], -1, 0
	s_add_u32 s49, s16, s10
	s_addc_u32 s50, s9, s11
	s_add_u32 s46, s8, s10
	s_addc_u32 s47, s3, s11
	s_add_u32 s20, s46, 0x100
	s_addc_u32 s48, s47, 0
	s_add_u32 s12, s49, 0x40080
	s_addc_u32 s0, s50, 0
	s_and_b32 s13, s0, 0xffff
	s_branch .LBB4_14
.LBB4_13:
	s_waitcnt vmcnt(6)
	s_barrier
	s_setprio 1
	v_mfma_f32_16x16x128_f8f6f4 v[116:119], v[24:31], v[56:63], v[116:119]
	s_add_i32 s44, s44, 2
	s_add_u32 s10, s10, 0x100
	s_addc_u32 s11, s11, 0
	v_mfma_f32_16x16x128_f8f6f4 v[112:115], v[16:23], v[56:63], v[112:115]
	s_cmpk_eq_i32 s10, 0x700
	s_cselect_b64 s[18:19], -1, 0
	s_cmpk_lg_i32 s10, 0x700
	s_cselect_b64 s[24:25], -1, 0
	v_mfma_f32_16x16x128_f8f6f4 v[100:103], v[24:31], v[48:55], v[100:103]
	s_add_u32 s49, s16, s10
	s_addc_u32 s50, s9, s11
	s_add_u32 s46, s8, s10
	s_addc_u32 s47, s3, s11
	v_mfma_f32_16x16x128_f8f6f4 v[96:99], v[16:23], v[48:55], v[96:99]
	s_add_u32 s20, s46, 0x100
	s_addc_u32 s48, s47, 0
	s_add_u32 s12, s49, 0x40080
	s_addc_u32 s0, s50, 0
	v_mfma_f32_16x16x128_f8f6f4 v[84:87], v[24:31], v[40:47], v[84:87]
	s_and_b32 s13, s0, 0xffff
	s_cmp_gt_u32 s44, 13
	v_mfma_f32_16x16x128_f8f6f4 v[80:83], v[16:23], v[40:47], v[80:83]
	v_mfma_f32_16x16x128_f8f6f4 v[68:71], v[24:31], v[32:39], v[68:71]
	v_mfma_f32_16x16x128_f8f6f4 v[64:67], v[16:23], v[32:39], v[64:67]
	s_setprio 0
	s_barrier
	s_cbranch_scc1 .LBB4_30
.LBB4_14:
	ds_read_b128 v[0:3], v202
	ds_read_b128 v[8:11], v202 offset:2048
	ds_read_b128 v[4:7], v203
	ds_read_b128 v[12:15], v203 offset:2048
	s_mov_b32 m0, s42
	ds_read_b128 v[56:59], v200
	ds_read_b128 v[48:51], v200 offset:2048
	ds_read_b128 v[60:63], v201
	ds_read_b128 v[52:55], v201 offset:2048
	ds_read_b128 v[40:43], v200 offset:4096
	ds_read_b128 v[32:35], v200 offset:6144
	ds_read_b128 v[44:47], v201 offset:4096
	ds_read_b128 v[36:39], v201 offset:6144
	buffer_load_dwordx4 v192, s[12:15], 0 offen lds
	s_mov_b32 m0, s43
	s_nop 0
	buffer_load_dwordx4 v194, s[12:15], 0 offen lds
	s_waitcnt lgkmcnt(8)
	s_barrier
	s_waitcnt lgkmcnt(0)
	s_setprio 1
	v_mfma_f32_16x16x128_f8f6f4 v[188:191], v[0:7], v[56:63], v[188:191]
	v_mfma_f32_16x16x128_f8f6f4 v[184:187], v[8:15], v[56:63], v[184:187]
	v_mfma_f32_16x16x128_f8f6f4 v[172:175], v[0:7], v[48:55], v[172:175]
	v_mfma_f32_16x16x128_f8f6f4 v[168:171], v[8:15], v[48:55], v[168:171]
	v_mfma_f32_16x16x128_f8f6f4 v[156:159], v[0:7], v[40:47], v[156:159]
	v_mfma_f32_16x16x128_f8f6f4 v[152:155], v[8:15], v[40:47], v[152:155]
	v_mfma_f32_16x16x128_f8f6f4 v[140:143], v[0:7], v[32:39], v[140:143]
	v_mfma_f32_16x16x128_f8f6f4 v[136:139], v[8:15], v[32:39], v[136:139]
	s_setprio 0
	s_barrier
	ds_read_b128 v[24:27], v204
	ds_read_b128 v[16:19], v204 offset:2048
	ds_read_b128 v[28:31], v205
	ds_read_b128 v[20:23], v205 offset:2048
	s_and_b64 vcc, exec, s[18:19]
	s_cbranch_vccnz .LBB4_16
	s_and_b32 s21, s48, 0xffff
	s_mov_b32 s22, s14
	s_mov_b32 s23, s15
	s_mov_b32 m0, s28
	s_nop 0
	buffer_load_dwordx4 v193, s[20:23], 0 offen lds
	s_mov_b32 m0, s29
	s_nop 0
	buffer_load_dwordx4 v195, s[20:23], 0 offen lds

.LBB5_16:
	s_and_b32 s35, s20, 3
	s_add_u32 s8, s12, 0x80
	s_load_dword s2, s[0:1], 0x48
	s_addc_u32 s0, s7, 0
	s_add_i32 s37, s25, 0x18000
	s_and_b32 s9, s0, 0xffff
	s_mov_b32 m0, s37
	s_add_i32 s38, s25, 0x1a000
	s_waitcnt vmcnt(4)
	s_barrier
	buffer_load_dwordx4 v192, s[8:11], 0 offen lds
	s_mov_b32 m0, s38
	v_lshrrev_b32_e32 v1, 4, v0
	buffer_load_dwordx4 v193, s[8:11], 0 offen lds
	s_add_u32 s8, s16, 0x80
	s_addc_u32 s0, s13, 0
	s_add_i32 s39, s25, 0x8000
	s_and_b32 s9, s0, 0xffff
	s_mov_b32 m0, s39
	s_add_i32 s40, s25, 0xa000
	buffer_load_dwordx4 v192, s[8:11], 0 offen lds
	s_mov_b32 m0, s40
	v_and_b32_e32 v194, 15, v0
	buffer_load_dwordx4 v193, s[8:11], 0 offen lds
	s_add_u32 s8, s12, 0x40080
	s_addc_u32 s0, s7, 0
	s_add_i32 s41, s25, 0x1c000
	s_and_b32 s9, s0, 0xffff
	s_mov_b32 m0, s41
	s_add_i32 s42, s25, 0x1e000
	buffer_load_dwordx4 v192, s[8:11], 0 offen lds
	s_mov_b32 m0, s42
	v_bfe_u32 v195, v0, 4, 2
	buffer_load_dwordx4 v193, s[8:11], 0 offen lds
	v_bfe_u32 v0, v0, 1, 3
	v_bitop3_b32 v0, v1, v0, 3 bitop3:0x6c
	v_lshlrev_b32_e32 v1, 7, v194
	v_lshlrev_b32_e32 v0, 4, v0
	v_lshl_or_b32 v2, s3, 13, v1
	v_lshl_or_b32 v1, s35, 12, v1
	s_waitcnt vmcnt(6)
	v_or_b32_e32 v3, v2, v0
	v_or_b32_e32 v196, v1, v0
	v_bitop3_b32 v2, v2, 64, v0 bitop3:0x36
	v_bitop3_b32 v197, v1, 64, v0 bitop3:0x36
	v_mov_b32_e32 v64, 0
	s_add_i32 s0, 0, 0x10000
	s_add_i32 s1, 0, 0x14000
	s_add_i32 s43, s25, 0xc000
	s_add_i32 s44, s25, 0xe000
	s_mov_b32 s45, -2
	s_mov_b64 s[14:15], 0
	v_add_u32_e32 v198, 0, v3
	v_add_u32_e32 v199, 0, v2
	s_add_i32 s46, 0, 0x18000
	v_mov_b32_e32 v65, v64
	v_mov_b32_e32 v66, v64
	v_mov_b32_e32 v67, v64
	v_mov_b32_e32 v68, v64
	v_mov_b32_e32 v69, v64
	v_mov_b32_e32 v70, v64
	v_mov_b32_e32 v71, v64
	v_mov_b32_e32 v76, v64
	v_mov_b32_e32 v77, v64
	v_mov_b32_e32 v78, v64
	v_mov_b32_e32 v79, v64
	v_mov_b32_e32 v80, v64
	v_mov_b32_e32 v81, v64
	v_mov_b32_e32 v82, v64
	v_mov_b32_e32 v83, v64
	v_mov_b32_e32 v88, v64
	v_mov_b32_e32 v89, v64
	v_mov_b32_e32 v90, v64
	v_mov_b32_e32 v91, v64
	v_mov_b32_e32 v92, v64
	v_mov_b32_e32 v93, v64
	v_mov_b32_e32 v94, v64
	v_mov_b32_e32 v95, v64
	v_mov_b32_e32 v104, v64
	v_mov_b32_e32 v105, v64
	v_mov_b32_e32 v106, v64
	v_mov_b32_e32 v107, v64
	v_mov_b32_e32 v108, v64
	v_mov_b32_e32 v109, v64
	v_mov_b32_e32 v110, v64
	v_mov_b32_e32 v111, v64
	v_mov_b32_e32 v72, v64
	v_mov_b32_e32 v73, v64
	v_mov_b32_e32 v74, v64
	v_mov_b32_e32 v75, v64
	v_mov_b32_e32 v84, v64
	v_mov_b32_e32 v85, v64
	v_mov_b32_e32 v86, v64
	v_mov_b32_e32 v87, v64
	v_mov_b32_e32 v96, v64
	v_mov_b32_e32 v97, v64
	v_mov_b32_e32 v98, v64
	v_mov_b32_e32 v99, v64
	v_mov_b32_e32 v100, v64
	v_mov_b32_e32 v101, v64
	v_mov_b32_e32 v102, v64
	v_mov_b32_e32 v103, v64
	v_mov_b32_e32 v112, v64
	v_mov_b32_e32 v113, v64
	v_mov_b32_e32 v114, v64
	v_mov_b32_e32 v115, v64
	v_mov_b32_e32 v116, v64
	v_mov_b32_e32 v117, v64
	v_mov_b32_e32 v118, v64
	v_mov_b32_e32 v119, v64
	v_mov_b32_e32 v120, v64
	v_mov_b32_e32 v121, v64
	v_mov_b32_e32 v122, v64
	v_mov_b32_e32 v123, v64
	v_mov_b32_e32 v124, v64
	v_mov_b32_e32 v125, v64
	v_mov_b32_e32 v126, v64
	v_mov_b32_e32 v127, v64
	v_mov_b32_e32 v128, v64
	v_mov_b32_e32 v129, v64
	v_mov_b32_e32 v130, v64
	v_mov_b32_e32 v131, v64
	v_mov_b32_e32 v132, v64
	v_mov_b32_e32 v133, v64
	v_mov_b32_e32 v134, v64
	v_mov_b32_e32 v135, v64
	v_mov_b32_e32 v140, v64
	v_mov_b32_e32 v141, v64
	v_mov_b32_e32 v142, v64
	v_mov_b32_e32 v143, v64
	v_mov_b32_e32 v148, v64
	v_mov_b32_e32 v149, v64
	v_mov_b32_e32 v150, v64
	v_mov_b32_e32 v151, v64
	v_mov_b32_e32 v156, v64
	v_mov_b32_e32 v157, v64
	v_mov_b32_e32 v158, v64
	v_mov_b32_e32 v159, v64
	v_mov_b32_e32 v164, v64
	v_mov_b32_e32 v165, v64
	v_mov_b32_e32 v166, v64
	v_mov_b32_e32 v167, v64
	v_mov_b32_e32 v172, v64
	v_mov_b32_e32 v173, v64
	v_mov_b32_e32 v174, v64
	v_mov_b32_e32 v175, v64
	v_mov_b32_e32 v180, v64
	v_mov_b32_e32 v181, v64
	v_mov_b32_e32 v182, v64
	v_mov_b32_e32 v183, v64
	v_mov_b32_e32 v136, v64
	v_mov_b32_e32 v137, v64
	v_mov_b32_e32 v138, v64
	v_mov_b32_e32 v139, v64
	v_mov_b32_e32 v144, v64
	v_mov_b32_e32 v145, v64
	v_mov_b32_e32 v146, v64
	v_mov_b32_e32 v147, v64
	v_mov_b32_e32 v152, v64
	v_mov_b32_e32 v153, v64
	v_mov_b32_e32 v154, v64
	v_mov_b32_e32 v155, v64
	v_mov_b32_e32 v160, v64
	v_mov_b32_e32 v161, v64
	v_mov_b32_e32 v162, v64
	v_mov_b32_e32 v163, v64
	v_mov_b32_e32 v168, v64
	v_mov_b32_e32 v169, v64
	v_mov_b32_e32 v170, v64
	v_mov_b32_e32 v171, v64
	v_mov_b32_e32 v176, v64
	v_mov_b32_e32 v177, v64
	v_mov_b32_e32 v178, v64
	v_mov_b32_e32 v179, v64
	v_mov_b32_e32 v184, v64
	v_mov_b32_e32 v185, v64
	v_mov_b32_e32 v186, v64
	v_mov_b32_e32 v187, v64
	v_mov_b32_e32 v188, v64
	v_mov_b32_e32 v189, v64
	v_mov_b32_e32 v190, v64
	v_mov_b32_e32 v191, v64
	v_add_u32_e32 v200, s0, v196
	v_add_u32_e32 v201, s0, v197
	v_add_u32_e32 v202, s1, v196
	v_add_u32_e32 v203, s1, v197
	s_barrier
	s_cmpk_eq_i32 s14, 0x700
	s_cselect_b64 s[18:19], -1, 0
	s_cmpk_lg_i32 s14, 0x700
	s_cselect_b64 s[26:27], -1, 0
	s_add_u32 s50, s16, s14
	s_addc_u32 s51, s13, s15
	s_add_u32 s47, s12, s14
	s_addc_u32 s48, s7, s15
	s_add_u32 s20, s47, 0x100
	s_addc_u32 s49, s48, 0
	s_add_u32 s8, s50, 0x40080
	s_addc_u32 s0, s51, 0
	s_and_b32 s9, s0, 0xffff
	s_branch .LBB5_18
.LBB5_17:
	s_waitcnt vmcnt(6)
	s_barrier
	s_setprio 1
	v_mfma_f32_16x16x128_f8f6f4 v[108:111], v[24:31], v[56:63], v[108:111]
	s_add_i32 s45, s45, 2
	s_add_u32 s14, s14, 0x100
	s_addc_u32 s15, s15, 0
	v_mfma_f32_16x16x128_f8f6f4 v[104:107], v[16:23], v[56:63], v[104:107]
	s_cmpk_eq_i32 s14, 0x700
	s_cselect_b64 s[18:19], -1, 0
	s_cmpk_lg_i32 s14, 0x700
	s_cselect_b64 s[26:27], -1, 0
	v_mfma_f32_16x16x128_f8f6f4 v[92:95], v[24:31], v[48:55], v[92:95]
	s_add_u32 s50, s16, s14
	s_addc_u32 s51, s13, s15
	s_add_u32 s47, s12, s14
	s_addc_u32 s48, s7, s15
	v_mfma_f32_16x16x128_f8f6f4 v[88:91], v[16:23], v[48:55], v[88:91]
	s_add_u32 s20, s47, 0x100
	s_addc_u32 s49, s48, 0
	s_add_u32 s8, s50, 0x40080
	s_addc_u32 s0, s51, 0
	v_mfma_f32_16x16x128_f8f6f4 v[80:83], v[24:31], v[40:47], v[80:83]
	s_and_b32 s9, s0, 0xffff
	s_cmp_gt_u32 s45, 13
	v_mfma_f32_16x16x128_f8f6f4 v[76:79], v[16:23], v[40:47], v[76:79]
	v_mfma_f32_16x16x128_f8f6f4 v[68:71], v[24:31], v[32:39], v[68:71]
	v_mfma_f32_16x16x128_f8f6f4 v[64:67], v[16:23], v[32:39], v[64:67]
	s_setprio 0
	s_barrier
	s_cbranch_scc1 .LBB5_34
.LBB5_18:
	ds_read_b128 v[0:3], v200
	ds_read_b128 v[8:11], v200 offset:2048
	ds_read_b128 v[4:7], v201
	ds_read_b128 v[12:15], v201 offset:2048
	s_mov_b32 m0, s43
	ds_read_b128 v[56:59], v198
	ds_read_b128 v[48:51], v198 offset:2048
	ds_read_b128 v[60:63], v199
	ds_read_b128 v[52:55], v199 offset:2048
	ds_read_b128 v[40:43], v198 offset:4096
	ds_read_b128 v[32:35], v198 offset:6144
	ds_read_b128 v[44:47], v199 offset:4096
	ds_read_b128 v[36:39], v199 offset:6144
	buffer_load_dwordx4 v192, s[8:11], 0 offen lds
	s_mov_b32 m0, s44
	s_nop 0
	buffer_load_dwordx4 v193, s[8:11], 0 offen lds
	s_waitcnt lgkmcnt(8)
	s_barrier
	s_waitcnt lgkmcnt(0)
	s_setprio 1
	v_mfma_f32_16x16x128_f8f6f4 v[188:191], v[0:7], v[56:63], v[188:191]
	v_mfma_f32_16x16x128_f8f6f4 v[184:187], v[8:15], v[56:63], v[184:187]
	v_mfma_f32_16x16x128_f8f6f4 v[176:179], v[0:7], v[48:55], v[176:179]
	v_mfma_f32_16x16x128_f8f6f4 v[168:171], v[8:15], v[48:55], v[168:171]
	v_mfma_f32_16x16x128_f8f6f4 v[160:163], v[0:7], v[40:47], v[160:163]
	v_mfma_f32_16x16x128_f8f6f4 v[152:155], v[8:15], v[40:47], v[152:155]
	v_mfma_f32_16x16x128_f8f6f4 v[144:147], v[0:7], v[32:39], v[144:147]
	v_mfma_f32_16x16x128_f8f6f4 v[136:139], v[8:15], v[32:39], v[136:139]
	s_setprio 0
	s_barrier
	ds_read_b128 v[24:27], v202
	ds_read_b128 v[16:19], v202 offset:2048
	ds_read_b128 v[28:31], v203
	ds_read_b128 v[20:23], v203 offset:2048
	s_and_b64 vcc, exec, s[18:19]
	s_cbranch_vccnz .LBB5_20
	s_and_b32 s21, s49, 0xffff
	s_mov_b32 s22, s10
	s_mov_b32 s23, s11
	s_mov_b32 m0, s29
	s_nop 0
	buffer_load_dwordx4 v192, s[20:23], 0 offen lds
	s_mov_b32 m0, s30
	s_nop 0
	buffer_load_dwordx4 v193, s[20:23], 0 offen lds
